# S5 Toeplitz precompute loop rewritten (W hoisted, 16 acc in regs), prologue rows rebalanced 2:14, nt conv stores, per_light 22/14
# speedup vs baseline: 1.0118x; 1.0118x over previous
; __device__ __forceinline__ void s5_precompute_group(const Ctx& c, int g) {
;     ...
;     for (int idx = tid; idx < 16 * 32 * 16; idx += NTHR) {
;         const int co = idx >> 9, tau = (idx >> 4) & 31, ci = idx & 15; float acc = 0.f;
;         for (int p = 0; p < 64; ++p) { const float pr = PR[tau * 64 + p], pi = PI[tau * 64 + p], br = BBR[p * 16 + ci], bi = BBI[p * 16 + ci];
;             const float wr = pr * br - pi * bi, wi = pr * bi + pi * br; acc += CRE[co * 64 + p] * wr - CIM[co * 64 + p] * wi; }
;         Rg[co * 1024 + (31 - tau) * 16 + ci] = f2bf(acc);
;     }
.LBB0_38:
	s_or_b64 exec, exec, s[18:19]
	v_lshlrev_b64 v[20:21], 15, v[18:19]
	v_lshl_add_u64 v[20:21], s[34:35], 0, v[20:21]
	s_waitcnt lgkmcnt(0)
	s_barrier
	s_and_saveexec_b64 s[18:19], s[6:7]
	s_cbranch_execz .LBB0_43
	v_lshlrev_b32_e32 v84, 4, v8
	v_and_b32_e32 v84, 0x1f00, v84
	v_add_u32_e32 v84, s25, v84
	ds_read_b128 v[88:91], v84 offset:0
	ds_read_b128 v[92:95], v84 offset:8448
	ds_read_b32 v228, v27 offset:0
	ds_read_b32 v232, v27 offset:4096
	ds_read_b32 v229, v27 offset:64
	ds_read_b32 v233, v27 offset:4160
	ds_read_b32 v230, v27 offset:128
	ds_read_b32 v234, v27 offset:4224
	ds_read_b32 v231, v27 offset:192
	ds_read_b32 v235, v27 offset:4288
	s_waitcnt lgkmcnt(0)
	v_mul_f32_e32 v100, v88, v228
	v_mul_f32_e32 v164, v88, v232
	v_mul_f32_e32 v101, v89, v229
	v_mul_f32_e32 v165, v89, v233
	v_mul_f32_e32 v102, v90, v230
	v_mul_f32_e32 v166, v90, v234
	v_mul_f32_e32 v103, v91, v231
	v_mul_f32_e32 v167, v91, v235
	v_fma_f32 v100, -v92, v232, v100
	v_fmac_f32_e32 v164, v92, v228
	v_fma_f32 v101, -v93, v233, v101
	v_fmac_f32_e32 v165, v93, v229
	v_fma_f32 v102, -v94, v234, v102
	v_fmac_f32_e32 v166, v94, v230
	v_fma_f32 v103, -v95, v235, v103
	v_fmac_f32_e32 v167, v95, v231
	ds_read_b128 v[88:91], v84 offset:16
	ds_read_b128 v[92:95], v84 offset:8464
	ds_read_b32 v228, v27 offset:256
	ds_read_b32 v232, v27 offset:4352
	ds_read_b32 v229, v27 offset:320
	ds_read_b32 v233, v27 offset:4416
	ds_read_b32 v230, v27 offset:384
	ds_read_b32 v234, v27 offset:4480
	ds_read_b32 v231, v27 offset:448
	ds_read_b32 v235, v27 offset:4544
	s_waitcnt lgkmcnt(0)
	v_mul_f32_e32 v104, v88, v228
	v_mul_f32_e32 v168, v88, v232
	v_mul_f32_e32 v105, v89, v229
	v_mul_f32_e32 v169, v89, v233
	v_mul_f32_e32 v106, v90, v230
	v_mul_f32_e32 v170, v90, v234
	v_mul_f32_e32 v107, v91, v231
	v_mul_f32_e32 v171, v91, v235
	v_fma_f32 v104, -v92, v232, v104
	v_fmac_f32_e32 v168, v92, v228
	v_fma_f32 v105, -v93, v233, v105
	v_fmac_f32_e32 v169, v93, v229
	v_fma_f32 v106, -v94, v234, v106
	v_fmac_f32_e32 v170, v94, v230
	v_fma_f32 v107, -v95, v235, v107
	v_fmac_f32_e32 v171, v95, v231
	ds_read_b128 v[88:91], v84 offset:32
	ds_read_b128 v[92:95], v84 offset:8480
	ds_read_b32 v228, v27 offset:512
	ds_read_b32 v232, v27 offset:4608
	ds_read_b32 v229, v27 offset:576
	ds_read_b32 v233, v27 offset:4672
	ds_read_b32 v230, v27 offset:640
	ds_read_b32 v234, v27 offset:4736
	ds_read_b32 v231, v27 offset:704
	ds_read_b32 v235, v27 offset:4800
	s_waitcnt lgkmcnt(0)
	v_mul_f32_e32 v108, v88, v228
	v_mul_f32_e32 v172, v88, v232
	v_mul_f32_e32 v109, v89, v229
	v_mul_f32_e32 v173, v89, v233
	v_mul_f32_e32 v110, v90, v230
	v_mul_f32_e32 v174, v90, v234
	v_mul_f32_e32 v111, v91, v231
	v_mul_f32_e32 v175, v91, v235
	v_fma_f32 v108, -v92, v232, v108
	v_fmac_f32_e32 v172, v92, v228
	v_fma_f32 v109, -v93, v233, v109
	v_fmac_f32_e32 v173, v93, v229
	v_fma_f32 v110, -v94, v234, v110
	v_fmac_f32_e32 v174, v94, v230
	v_fma_f32 v111, -v95, v235, v111
	v_fmac_f32_e32 v175, v95, v231
	ds_read_b128 v[88:91], v84 offset:48
	ds_read_b128 v[92:95], v84 offset:8496
	ds_read_b32 v228, v27 offset:768
	ds_read_b32 v232, v27 offset:4864
	ds_read_b32 v229, v27 offset:832
	ds_read_b32 v233, v27 offset:4928
	ds_read_b32 v230, v27 offset:896
	ds_read_b32 v234, v27 offset:4992
	ds_read_b32 v231, v27 offset:960
	ds_read_b32 v235, v27 offset:5056
	s_waitcnt lgkmcnt(0)
	v_mul_f32_e32 v112, v88, v228
	v_mul_f32_e32 v176, v88, v232
	v_mul_f32_e32 v113, v89, v229
	v_mul_f32_e32 v177, v89, v233
	v_mul_f32_e32 v114, v90, v230
	v_mul_f32_e32 v178, v90, v234
	v_mul_f32_e32 v115, v91, v231
	v_mul_f32_e32 v179, v91, v235
	v_fma_f32 v112, -v92, v232, v112
	v_fmac_f32_e32 v176, v92, v228
	v_fma_f32 v113, -v93, v233, v113
	v_fmac_f32_e32 v177, v93, v229
	v_fma_f32 v114, -v94, v234, v114
	v_fmac_f32_e32 v178, v94, v230
	v_fma_f32 v115, -v95, v235, v115
	v_fmac_f32_e32 v179, v95, v231
	ds_read_b128 v[88:91], v84 offset:64
	ds_read_b128 v[92:95], v84 offset:8512
	ds_read_b32 v228, v27 offset:1024
	ds_read_b32 v232, v27 offset:5120
	ds_read_b32 v229, v27 offset:1088
	ds_read_b32 v233, v27 offset:5184
	ds_read_b32 v230, v27 offset:1152
	ds_read_b32 v234, v27 offset:5248
	ds_read_b32 v231, v27 offset:1216
	ds_read_b32 v235, v27 offset:5312
	s_waitcnt lgkmcnt(0)
	v_mul_f32_e32 v116, v88, v228
	v_mul_f32_e32 v180, v88, v232
	v_mul_f32_e32 v117, v89, v229
	v_mul_f32_e32 v181, v89, v233
	v_mul_f32_e32 v118, v90, v230
	v_mul_f32_e32 v182, v90, v234
	v_mul_f32_e32 v119, v91, v231
	v_mul_f32_e32 v183, v91, v235
	v_fma_f32 v116, -v92, v232, v116
	v_fmac_f32_e32 v180, v92, v228
	v_fma_f32 v117, -v93, v233, v117
	v_fmac_f32_e32 v181, v93, v229
	v_fma_f32 v118, -v94, v234, v118
	v_fmac_f32_e32 v182, v94, v230
	v_fma_f32 v119, -v95, v235, v119
	v_fmac_f32_e32 v183, v95, v231
	ds_read_b128 v[88:91], v84 offset:80
	ds_read_b128 v[92:95], v84 offset:8528
	ds_read_b32 v228, v27 offset:1280
	ds_read_b32 v232, v27 offset:5376
	ds_read_b32 v229, v27 offset:1344
	ds_read_b32 v233, v27 offset:5440
	ds_read_b32 v230, v27 offset:1408
	ds_read_b32 v234, v27 offset:5504
	ds_read_b32 v231, v27 offset:1472
	ds_read_b32 v235, v27 offset:5568
	s_waitcnt lgkmcnt(0)
	v_mul_f32_e32 v120, v88, v228
	v_mul_f32_e32 v184, v88, v232
	v_mul_f32_e32 v121, v89, v229
	v_mul_f32_e32 v185, v89, v233
	v_mul_f32_e32 v122, v90, v230
	v_mul_f32_e32 v186, v90, v234
	v_mul_f32_e32 v123, v91, v231
	v_mul_f32_e32 v187, v91, v235
	v_fma_f32 v120, -v92, v232, v120
	v_fmac_f32_e32 v184, v92, v228
	v_fma_f32 v121, -v93, v233, v121
	v_fmac_f32_e32 v185, v93, v229
	v_fma_f32 v122, -v94, v234, v122
	v_fmac_f32_e32 v186, v94, v230
	v_fma_f32 v123, -v95, v235, v123
	v_fmac_f32_e32 v187, v95, v231
	ds_read_b128 v[88:91], v84 offset:96
	ds_read_b128 v[92:95], v84 offset:8544
	ds_read_b32 v228, v27 offset:1536
	ds_read_b32 v232, v27 offset:5632
	ds_read_b32 v229, v27 offset:1600
	ds_read_b32 v233, v27 offset:5696
	ds_read_b32 v230, v27 offset:1664
	ds_read_b32 v234, v27 offset:5760
	ds_read_b32 v231, v27 offset:1728
	ds_read_b32 v235, v27 offset:5824
	s_waitcnt lgkmcnt(0)
; __device__ __forceinline__ void s5_precompute_group(const Ctx& c, int g) {
;     ...
;     for (int idx = tid; idx < 16 * 32 * 16; idx += NTHR) {
;         const int co = idx >> 9, tau = (idx >> 4) & 31, ci = idx & 15; float acc = 0.f;
;         for (int p = 0; p < 64; ++p) { const float pr = PR[tau * 64 + p], pi = PI[tau * 64 + p], br = BBR[p * 16 + ci], bi = BBI[p * 16 + ci];
;             const float wr = pr * br - pi * bi, wi = pr * bi + pi * br; acc += CRE[co * 64 + p] * wr - CIM[co * 64 + p] * wi; }
;         Rg[co * 1024 + (31 - tau) * 16 + ci] = f2bf(acc);
;     }
	v_mul_f32_e32 v124, v88, v228
	v_mul_f32_e32 v188, v88, v232
	v_mul_f32_e32 v125, v89, v229
	v_mul_f32_e32 v189, v89, v233
	v_mul_f32_e32 v126, v90, v230
	v_mul_f32_e32 v190, v90, v234
	v_mul_f32_e32 v127, v91, v231
	v_mul_f32_e32 v191, v91, v235
	v_fma_f32 v124, -v92, v232, v124
	v_fmac_f32_e32 v188, v92, v228
	v_fma_f32 v125, -v93, v233, v125
	v_fmac_f32_e32 v189, v93, v229
	v_fma_f32 v126, -v94, v234, v126
	v_fmac_f32_e32 v190, v94, v230
	v_fma_f32 v127, -v95, v235, v127
	v_fmac_f32_e32 v191, v95, v231
	ds_read_b128 v[88:91], v84 offset:112
	ds_read_b128 v[92:95], v84 offset:8560
	ds_read_b32 v228, v27 offset:1792
	ds_read_b32 v232, v27 offset:5888
	ds_read_b32 v229, v27 offset:1856
	ds_read_b32 v233, v27 offset:5952
	ds_read_b32 v230, v27 offset:1920
	ds_read_b32 v234, v27 offset:6016
	ds_read_b32 v231, v27 offset:1984
	ds_read_b32 v235, v27 offset:6080
	s_waitcnt lgkmcnt(0)
	v_mul_f32_e32 v128, v88, v228
	v_mul_f32_e32 v192, v88, v232
	v_mul_f32_e32 v129, v89, v229
	v_mul_f32_e32 v193, v89, v233
	v_mul_f32_e32 v130, v90, v230
	v_mul_f32_e32 v194, v90, v234
	v_mul_f32_e32 v131, v91, v231
	v_mul_f32_e32 v195, v91, v235
	v_fma_f32 v128, -v92, v232, v128
	v_fmac_f32_e32 v192, v92, v228
	v_fma_f32 v129, -v93, v233, v129
	v_fmac_f32_e32 v193, v93, v229
	v_fma_f32 v130, -v94, v234, v130
	v_fmac_f32_e32 v194, v94, v230
	v_fma_f32 v131, -v95, v235, v131
	v_fmac_f32_e32 v195, v95, v231
	ds_read_b128 v[88:91], v84 offset:128
	ds_read_b128 v[92:95], v84 offset:8576
	ds_read_b32 v228, v27 offset:2048
	ds_read_b32 v232, v27 offset:6144
	ds_read_b32 v229, v27 offset:2112
	ds_read_b32 v233, v27 offset:6208
	ds_read_b32 v230, v27 offset:2176
	ds_read_b32 v234, v27 offset:6272
	ds_read_b32 v231, v27 offset:2240
	ds_read_b32 v235, v27 offset:6336
	s_waitcnt lgkmcnt(0)
	v_mul_f32_e32 v132, v88, v228
	v_mul_f32_e32 v196, v88, v232
	v_mul_f32_e32 v133, v89, v229
	v_mul_f32_e32 v197, v89, v233
	v_mul_f32_e32 v134, v90, v230
	v_mul_f32_e32 v198, v90, v234
	v_mul_f32_e32 v135, v91, v231
	v_mul_f32_e32 v199, v91, v235
	v_fma_f32 v132, -v92, v232, v132
	v_fmac_f32_e32 v196, v92, v228
	v_fma_f32 v133, -v93, v233, v133
	v_fmac_f32_e32 v197, v93, v229
	v_fma_f32 v134, -v94, v234, v134
	v_fmac_f32_e32 v198, v94, v230
	v_fma_f32 v135, -v95, v235, v135
	v_fmac_f32_e32 v199, v95, v231
	ds_read_b128 v[88:91], v84 offset:144
	ds_read_b128 v[92:95], v84 offset:8592
	ds_read_b32 v228, v27 offset:2304
	ds_read_b32 v232, v27 offset:6400
	ds_read_b32 v229, v27 offset:2368
	ds_read_b32 v233, v27 offset:6464
	ds_read_b32 v230, v27 offset:2432
	ds_read_b32 v234, v27 offset:6528
	ds_read_b32 v231, v27 offset:2496
	ds_read_b32 v235, v27 offset:6592
	s_waitcnt lgkmcnt(0)
	v_mul_f32_e32 v136, v88, v228
	v_mul_f32_e32 v200, v88, v232
	v_mul_f32_e32 v137, v89, v229
	v_mul_f32_e32 v201, v89, v233
	v_mul_f32_e32 v138, v90, v230
	v_mul_f32_e32 v202, v90, v234
	v_mul_f32_e32 v139, v91, v231
	v_mul_f32_e32 v203, v91, v235
	v_fma_f32 v136, -v92, v232, v136
	v_fmac_f32_e32 v200, v92, v228
	v_fma_f32 v137, -v93, v233, v137
	v_fmac_f32_e32 v201, v93, v229
	v_fma_f32 v138, -v94, v234, v138
	v_fmac_f32_e32 v202, v94, v230
	v_fma_f32 v139, -v95, v235, v139
	v_fmac_f32_e32 v203, v95, v231
	ds_read_b128 v[88:91], v84 offset:160
	ds_read_b128 v[92:95], v84 offset:8608
	ds_read_b32 v228, v27 offset:2560
	ds_read_b32 v232, v27 offset:6656
	ds_read_b32 v229, v27 offset:2624
	ds_read_b32 v233, v27 offset:6720
	ds_read_b32 v230, v27 offset:2688
	ds_read_b32 v234, v27 offset:6784
	ds_read_b32 v231, v27 offset:2752
	ds_read_b32 v235, v27 offset:6848
	s_waitcnt lgkmcnt(0)
	v_mul_f32_e32 v140, v88, v228
	v_mul_f32_e32 v204, v88, v232
	v_mul_f32_e32 v141, v89, v229
	v_mul_f32_e32 v205, v89, v233
	v_mul_f32_e32 v142, v90, v230
	v_mul_f32_e32 v206, v90, v234
	v_mul_f32_e32 v143, v91, v231
	v_mul_f32_e32 v207, v91, v235
	v_fma_f32 v140, -v92, v232, v140
	v_fmac_f32_e32 v204, v92, v228
	v_fma_f32 v141, -v93, v233, v141
	v_fmac_f32_e32 v205, v93, v229
	v_fma_f32 v142, -v94, v234, v142
	v_fmac_f32_e32 v206, v94, v230
	v_fma_f32 v143, -v95, v235, v143
	v_fmac_f32_e32 v207, v95, v231
	ds_read_b128 v[88:91], v84 offset:176
	ds_read_b128 v[92:95], v84 offset:8624
	ds_read_b32 v228, v27 offset:2816
	ds_read_b32 v232, v27 offset:6912
	ds_read_b32 v229, v27 offset:2880
	ds_read_b32 v233, v27 offset:6976
	ds_read_b32 v230, v27 offset:2944
	ds_read_b32 v234, v27 offset:7040
	ds_read_b32 v231, v27 offset:3008
	ds_read_b32 v235, v27 offset:7104
	s_waitcnt lgkmcnt(0)
	v_mul_f32_e32 v144, v88, v228
	v_mul_f32_e32 v208, v88, v232
	v_mul_f32_e32 v145, v89, v229
	v_mul_f32_e32 v209, v89, v233
	v_mul_f32_e32 v146, v90, v230
	v_mul_f32_e32 v210, v90, v234
	v_mul_f32_e32 v147, v91, v231
	v_mul_f32_e32 v211, v91, v235
	v_fma_f32 v144, -v92, v232, v144
	v_fmac_f32_e32 v208, v92, v228
	v_fma_f32 v145, -v93, v233, v145
	v_fmac_f32_e32 v209, v93, v229
	v_fma_f32 v146, -v94, v234, v146
	v_fmac_f32_e32 v210, v94, v230
	v_fma_f32 v147, -v95, v235, v147
	v_fmac_f32_e32 v211, v95, v231
	ds_read_b128 v[88:91], v84 offset:192
	ds_read_b128 v[92:95], v84 offset:8640
	ds_read_b32 v228, v27 offset:3072
	ds_read_b32 v232, v27 offset:7168
	ds_read_b32 v229, v27 offset:3136
	ds_read_b32 v233, v27 offset:7232
	ds_read_b32 v230, v27 offset:3200
	ds_read_b32 v234, v27 offset:7296
	ds_read_b32 v231, v27 offset:3264
	ds_read_b32 v235, v27 offset:7360
	s_waitcnt lgkmcnt(0)
; __device__ __forceinline__ void s5_precompute_group(const Ctx& c, int g) {
;     ...
;     for (int idx = tid; idx < 16 * 32 * 16; idx += NTHR) {
;         const int co = idx >> 9, tau = (idx >> 4) & 31, ci = idx & 15; float acc = 0.f;
;         for (int p = 0; p < 64; ++p) { const float pr = PR[tau * 64 + p], pi = PI[tau * 64 + p], br = BBR[p * 16 + ci], bi = BBI[p * 16 + ci];
;             const float wr = pr * br - pi * bi, wi = pr * bi + pi * br; acc += CRE[co * 64 + p] * wr - CIM[co * 64 + p] * wi; }
;         Rg[co * 1024 + (31 - tau) * 16 + ci] = f2bf(acc);
;     }
	v_mul_f32_e32 v148, v88, v228
	v_mul_f32_e32 v212, v88, v232
	v_mul_f32_e32 v149, v89, v229
	v_mul_f32_e32 v213, v89, v233
	v_mul_f32_e32 v150, v90, v230
	v_mul_f32_e32 v214, v90, v234
	v_mul_f32_e32 v151, v91, v231
	v_mul_f32_e32 v215, v91, v235
	v_fma_f32 v148, -v92, v232, v148
	v_fmac_f32_e32 v212, v92, v228
	v_fma_f32 v149, -v93, v233, v149
	v_fmac_f32_e32 v213, v93, v229
	v_fma_f32 v150, -v94, v234, v150
	v_fmac_f32_e32 v214, v94, v230
	v_fma_f32 v151, -v95, v235, v151
	v_fmac_f32_e32 v215, v95, v231
	ds_read_b128 v[88:91], v84 offset:208
	ds_read_b128 v[92:95], v84 offset:8656
	ds_read_b32 v228, v27 offset:3328
	ds_read_b32 v232, v27 offset:7424
	ds_read_b32 v229, v27 offset:3392
	ds_read_b32 v233, v27 offset:7488
	ds_read_b32 v230, v27 offset:3456
	ds_read_b32 v234, v27 offset:7552
	ds_read_b32 v231, v27 offset:3520
	ds_read_b32 v235, v27 offset:7616
	s_waitcnt lgkmcnt(0)
	v_mul_f32_e32 v152, v88, v228
	v_mul_f32_e32 v216, v88, v232
	v_mul_f32_e32 v153, v89, v229
	v_mul_f32_e32 v217, v89, v233
	v_mul_f32_e32 v154, v90, v230
	v_mul_f32_e32 v218, v90, v234
	v_mul_f32_e32 v155, v91, v231
	v_mul_f32_e32 v219, v91, v235
	v_fma_f32 v152, -v92, v232, v152
	v_fmac_f32_e32 v216, v92, v228
	v_fma_f32 v153, -v93, v233, v153
	v_fmac_f32_e32 v217, v93, v229
	v_fma_f32 v154, -v94, v234, v154
	v_fmac_f32_e32 v218, v94, v230
	v_fma_f32 v155, -v95, v235, v155
	v_fmac_f32_e32 v219, v95, v231
	ds_read_b128 v[88:91], v84 offset:224
	ds_read_b128 v[92:95], v84 offset:8672
	ds_read_b32 v228, v27 offset:3584
	ds_read_b32 v232, v27 offset:7680
	ds_read_b32 v229, v27 offset:3648
	ds_read_b32 v233, v27 offset:7744
	ds_read_b32 v230, v27 offset:3712
	ds_read_b32 v234, v27 offset:7808
	ds_read_b32 v231, v27 offset:3776
	ds_read_b32 v235, v27 offset:7872
	s_waitcnt lgkmcnt(0)
	v_mul_f32_e32 v156, v88, v228
	v_mul_f32_e32 v220, v88, v232
	v_mul_f32_e32 v157, v89, v229
	v_mul_f32_e32 v221, v89, v233
	v_mul_f32_e32 v158, v90, v230
	v_mul_f32_e32 v222, v90, v234
	v_mul_f32_e32 v159, v91, v231
	v_mul_f32_e32 v223, v91, v235
	v_fma_f32 v156, -v92, v232, v156
	v_fmac_f32_e32 v220, v92, v228
	v_fma_f32 v157, -v93, v233, v157
	v_fmac_f32_e32 v221, v93, v229
	v_fma_f32 v158, -v94, v234, v158
	v_fmac_f32_e32 v222, v94, v230
	v_fma_f32 v159, -v95, v235, v159
	v_fmac_f32_e32 v223, v95, v231
	ds_read_b128 v[88:91], v84 offset:240
	ds_read_b128 v[92:95], v84 offset:8688
	ds_read_b32 v228, v27 offset:3840
	ds_read_b32 v232, v27 offset:7936
	ds_read_b32 v229, v27 offset:3904
	ds_read_b32 v233, v27 offset:8000
	ds_read_b32 v230, v27 offset:3968
	ds_read_b32 v234, v27 offset:8064
	ds_read_b32 v231, v27 offset:4032
	ds_read_b32 v235, v27 offset:8128
	s_waitcnt lgkmcnt(0)
	v_mul_f32_e32 v160, v88, v228
	v_mul_f32_e32 v224, v88, v232
	v_mul_f32_e32 v161, v89, v229
	v_mul_f32_e32 v225, v89, v233
	v_mul_f32_e32 v162, v90, v230
	v_mul_f32_e32 v226, v90, v234
	v_mul_f32_e32 v163, v91, v231
	v_mul_f32_e32 v227, v91, v235
	v_fma_f32 v160, -v92, v232, v160
	v_fmac_f32_e32 v224, v92, v228
	v_fma_f32 v161, -v93, v233, v161
	v_fmac_f32_e32 v225, v93, v229
	v_fma_f32 v162, -v94, v234, v162
	v_fmac_f32_e32 v226, v94, v230
	v_fma_f32 v163, -v95, v235, v163
	v_fmac_f32_e32 v227, v95, v231
	v_xor_b32_e32 v252, 0x1f0, v8
	v_mov_b32_e32 v253, 0
	v_lshl_add_u64 v[252:253], v[252:253], 1, v[20:21]
	s_add_i32 s22, 0, 0x6400
	v_mov_b32_e32 v84, s22
	s_mov_b32 s22, 0
; __device__ __forceinline__ void s5_precompute_group(const Ctx& c, int g) {
;     ...
;     for (int idx = tid; idx < 16 * 32 * 16; idx += NTHR) {
;         const int co = idx >> 9, tau = (idx >> 4) & 31, ci = idx & 15; float acc = 0.f;
;         for (int p = 0; p < 64; ++p) { const float pr = PR[tau * 64 + p], pi = PI[tau * 64 + p], br = BBR[p * 16 + ci], bi = BBI[p * 16 + ci];
;             const float wr = pr * br - pi * bi, wi = pr * bi + pi * br; acc += CRE[co * 64 + p] * wr - CIM[co * 64 + p] * wi; }
;         Rg[co * 1024 + (31 - tau) * 16 + ci] = f2bf(acc);
;     }
.Lrg_co:
	ds_read_b128 v[228:231], v84 offset:0
	ds_read_b128 v[232:235], v84 offset:4096
	ds_read_b128 v[236:239], v84 offset:16
	ds_read_b128 v[240:243], v84 offset:4112
	ds_read_b128 v[244:247], v84 offset:32
	ds_read_b128 v[248:251], v84 offset:4128
	v_mov_b32_e32 v96, 0
	v_mov_b32_e32 v97, 0
	v_mov_b32_e32 v98, 0
	v_mov_b32_e32 v99, 0
	ds_read_b128 v[88:91], v84 offset:48
	ds_read_b128 v[92:95], v84 offset:4144
	s_waitcnt lgkmcnt(6)
	v_fmac_f32_e32 v96, v228, v100
	v_fmac_f32_e32 v97, v229, v101
	v_fmac_f32_e32 v98, v230, v102
	v_fmac_f32_e32 v99, v231, v103
	v_fma_f32 v96, -v232, v164, v96
	v_fma_f32 v97, -v233, v165, v97
	v_fma_f32 v98, -v234, v166, v98
	v_fma_f32 v99, -v235, v167, v99
	ds_read_b128 v[228:231], v84 offset:64
	ds_read_b128 v[232:235], v84 offset:4160
	s_waitcnt lgkmcnt(6)
	v_fmac_f32_e32 v96, v236, v104
	v_fmac_f32_e32 v97, v237, v105
	v_fmac_f32_e32 v98, v238, v106
	v_fmac_f32_e32 v99, v239, v107
	v_fma_f32 v96, -v240, v168, v96
	v_fma_f32 v97, -v241, v169, v97
	v_fma_f32 v98, -v242, v170, v98
	v_fma_f32 v99, -v243, v171, v99
	ds_read_b128 v[236:239], v84 offset:80
	ds_read_b128 v[240:243], v84 offset:4176
	s_waitcnt lgkmcnt(6)
	v_fmac_f32_e32 v96, v244, v108
	v_fmac_f32_e32 v97, v245, v109
	v_fmac_f32_e32 v98, v246, v110
	v_fmac_f32_e32 v99, v247, v111
	v_fma_f32 v96, -v248, v172, v96
	v_fma_f32 v97, -v249, v173, v97
	v_fma_f32 v98, -v250, v174, v98
	v_fma_f32 v99, -v251, v175, v99
	ds_read_b128 v[244:247], v84 offset:96
	ds_read_b128 v[248:251], v84 offset:4192
	s_waitcnt lgkmcnt(6)
	v_fmac_f32_e32 v96, v88, v112
	v_fmac_f32_e32 v97, v89, v113
	v_fmac_f32_e32 v98, v90, v114
	v_fmac_f32_e32 v99, v91, v115
	v_fma_f32 v96, -v92, v176, v96
	v_fma_f32 v97, -v93, v177, v97
	v_fma_f32 v98, -v94, v178, v98
	v_fma_f32 v99, -v95, v179, v99
	ds_read_b128 v[88:91], v84 offset:112
	ds_read_b128 v[92:95], v84 offset:4208
	s_waitcnt lgkmcnt(6)
	v_fmac_f32_e32 v96, v228, v116
	v_fmac_f32_e32 v97, v229, v117
	v_fmac_f32_e32 v98, v230, v118
	v_fmac_f32_e32 v99, v231, v119
	v_fma_f32 v96, -v232, v180, v96
	v_fma_f32 v97, -v233, v181, v97
	v_fma_f32 v98, -v234, v182, v98
	v_fma_f32 v99, -v235, v183, v99
	ds_read_b128 v[228:231], v84 offset:128
	ds_read_b128 v[232:235], v84 offset:4224
	s_waitcnt lgkmcnt(6)
	v_fmac_f32_e32 v96, v236, v120
	v_fmac_f32_e32 v97, v237, v121
	v_fmac_f32_e32 v98, v238, v122
	v_fmac_f32_e32 v99, v239, v123
	v_fma_f32 v96, -v240, v184, v96
	v_fma_f32 v97, -v241, v185, v97
	v_fma_f32 v98, -v242, v186, v98
	v_fma_f32 v99, -v243, v187, v99
	ds_read_b128 v[236:239], v84 offset:144
	ds_read_b128 v[240:243], v84 offset:4240
	s_waitcnt lgkmcnt(6)
	v_fmac_f32_e32 v96, v244, v124
	v_fmac_f32_e32 v97, v245, v125
	v_fmac_f32_e32 v98, v246, v126
	v_fmac_f32_e32 v99, v247, v127
	v_fma_f32 v96, -v248, v188, v96
	v_fma_f32 v97, -v249, v189, v97
	v_fma_f32 v98, -v250, v190, v98
	v_fma_f32 v99, -v251, v191, v99
	ds_read_b128 v[244:247], v84 offset:160
	ds_read_b128 v[248:251], v84 offset:4256
	s_waitcnt lgkmcnt(6)
	v_fmac_f32_e32 v96, v88, v128
	v_fmac_f32_e32 v97, v89, v129
	v_fmac_f32_e32 v98, v90, v130
	v_fmac_f32_e32 v99, v91, v131
	v_fma_f32 v96, -v92, v192, v96
	v_fma_f32 v97, -v93, v193, v97
	v_fma_f32 v98, -v94, v194, v98
	v_fma_f32 v99, -v95, v195, v99
	ds_read_b128 v[88:91], v84 offset:176
	ds_read_b128 v[92:95], v84 offset:4272
	s_waitcnt lgkmcnt(6)
	v_fmac_f32_e32 v96, v228, v132
	v_fmac_f32_e32 v97, v229, v133
	v_fmac_f32_e32 v98, v230, v134
	v_fmac_f32_e32 v99, v231, v135
	v_fma_f32 v96, -v232, v196, v96
	v_fma_f32 v97, -v233, v197, v97
	v_fma_f32 v98, -v234, v198, v98
	v_fma_f32 v99, -v235, v199, v99
	ds_read_b128 v[228:231], v84 offset:192
	ds_read_b128 v[232:235], v84 offset:4288
	s_waitcnt lgkmcnt(6)
	v_fmac_f32_e32 v96, v236, v136
	v_fmac_f32_e32 v97, v237, v137
	v_fmac_f32_e32 v98, v238, v138
	v_fmac_f32_e32 v99, v239, v139
	v_fma_f32 v96, -v240, v200, v96
	v_fma_f32 v97, -v241, v201, v97
	v_fma_f32 v98, -v242, v202, v98
	v_fma_f32 v99, -v243, v203, v99
	ds_read_b128 v[236:239], v84 offset:208
	ds_read_b128 v[240:243], v84 offset:4304
	s_waitcnt lgkmcnt(6)
	v_fmac_f32_e32 v96, v244, v140
	v_fmac_f32_e32 v97, v245, v141
	v_fmac_f32_e32 v98, v246, v142
	v_fmac_f32_e32 v99, v247, v143
	v_fma_f32 v96, -v248, v204, v96
	v_fma_f32 v97, -v249, v205, v97
	v_fma_f32 v98, -v250, v206, v98
	v_fma_f32 v99, -v251, v207, v99
	ds_read_b128 v[244:247], v84 offset:224
	ds_read_b128 v[248:251], v84 offset:4320
	s_waitcnt lgkmcnt(6)
	v_fmac_f32_e32 v96, v88, v144
	v_fmac_f32_e32 v97, v89, v145
	v_fmac_f32_e32 v98, v90, v146
	v_fmac_f32_e32 v99, v91, v147
	v_fma_f32 v96, -v92, v208, v96
	v_fma_f32 v97, -v93, v209, v97
	v_fma_f32 v98, -v94, v210, v98
	v_fma_f32 v99, -v95, v211, v99
	ds_read_b128 v[88:91], v84 offset:240
	ds_read_b128 v[92:95], v84 offset:4336
	s_waitcnt lgkmcnt(6)
	v_fmac_f32_e32 v96, v228, v148
	v_fmac_f32_e32 v97, v229, v149
	v_fmac_f32_e32 v98, v230, v150
	v_fmac_f32_e32 v99, v231, v151
	v_fma_f32 v96, -v232, v212, v96
	v_fma_f32 v97, -v233, v213, v97
	v_fma_f32 v98, -v234, v214, v98
	v_fma_f32 v99, -v235, v215, v99
	s_waitcnt lgkmcnt(4)
	v_fmac_f32_e32 v96, v236, v152
	v_fmac_f32_e32 v97, v237, v153
	v_fmac_f32_e32 v98, v238, v154
	v_fmac_f32_e32 v99, v239, v155
	v_fma_f32 v96, -v240, v216, v96
	v_fma_f32 v97, -v241, v217, v97
	v_fma_f32 v98, -v242, v218, v98
	v_fma_f32 v99, -v243, v219, v99
	s_waitcnt lgkmcnt(2)
	v_fmac_f32_e32 v96, v244, v156
	v_fmac_f32_e32 v97, v245, v157
	v_fmac_f32_e32 v98, v246, v158
	v_fmac_f32_e32 v99, v247, v159
	v_fma_f32 v96, -v248, v220, v96
	v_fma_f32 v97, -v249, v221, v97
	v_fma_f32 v98, -v250, v222, v98
	v_fma_f32 v99, -v251, v223, v99
	s_waitcnt lgkmcnt(0)
	v_fmac_f32_e32 v96, v88, v160
	v_fmac_f32_e32 v97, v89, v161
	v_fmac_f32_e32 v98, v90, v162
	v_fmac_f32_e32 v99, v91, v163
	v_fma_f32 v96, -v92, v224, v96
	v_fma_f32 v97, -v93, v225, v97
	v_fma_f32 v98, -v94, v226, v98
	v_fma_f32 v99, -v95, v227, v99
	v_add_f32_e32 v96, v96, v97
	v_add_f32_e32 v98, v98, v99
	v_add_f32_e32 v96, v96, v98
	v_cvt_pk_bf16_f32 v85, v96, v96
	global_store_short v[252:253], v85, off
	v_add_co_u32_e32 v252, vcc, 0x800, v252
	v_add_u32_e32 v84, 0x100, v84
	s_nop 0
	v_addc_co_u32_e32 v253, vcc, 0, v253, vcc
	s_add_i32 s22, s22, 1
	s_cmp_lt_i32 s22, 16
	s_cbranch_scc1 .Lrg_co

; __device__ __forceinline__ void ph_prologue(const Ctx& c) {
;     ...
;         const bool bal = S5_MFMA && c.G == 256; const int heavy = c.bid < 128;
;         const int nrow = bal ? (heavy ? 6 : 10) : (T_ + c.G * NWAVE - 1) / (c.G * NWAVE);
;         const int row0 = bal ? (heavy ? (c.bid * NWAVE + c.wave) * 6 : 128 * NWAVE * 6 + ((c.bid - 128) * NWAVE + c.wave) * 10) : (c.bid * NWAVE + c.wave) * nrow;
.LBB0_156:
.LBB0_157:
	v_readlane_b32 s4, v254, 47
	v_readlane_b32 s5, v254, 48
	s_and_b64 s[4:5], s[4:5], exec
	s_cselect_b32 s3, 2, 14

; __device__ __forceinline__ void ph_prologue(const Ctx& c) {
;     ...
;         const int nrow = bal ? (heavy ? 6 : 10) : (T_ + c.G * NWAVE - 1) / (c.G * NWAVE);
;         const int row0 = bal ? (heavy ? (c.bid * NWAVE + c.wave) * 6 : 128 * NWAVE * 6 + ((c.bid - 128) * NWAVE + c.wave) * 10) : (c.bid * NWAVE + c.wave) * nrow;
.LBB0_160:
.LBB0_161:
	s_and_b64 vcc, exec, s[76:77]
	s_cbranch_vccz .LBB0_163
	v_readlane_b32 s0, v254, 46
	s_add_i32 s0, s6, s0
	s_mul_i32 s0, s0, 14
	s_addk_i32 s0, 0xd000
	s_cbranch_execz .LBB0_164
	s_branch .LBB0_165
.LBB0_163:
.LBB0_164:
	v_readlane_b32 s0, v254, 46
	s_add_i32 s0, s0, s6
	s_mul_i32 s0, s0, 2
